# h0 sweep: 16 x quads + 32 modulation quads requested up front, one wait, stores left in flight (was 16 dependent load/store round trips per sweep)
# baseline (speedup 1.0000x reference)
.LBB0_77:
	v_add_u32_e32 v93, s3, v92
	v_add_u32_e32 v90, s21, v92
	v_add_u32_e32 v88, s22, v92
	s_add_u32 s18, s78, 0x8500000
	s_addc_u32 s19, s79, 0
	s_add_u32 s4, s96, 0x1000
	s_addc_u32 s5, s97, 0
	v_lshl_add_u32 v94, v92, 12, v64
	v_ashrrev_i32_e32 v106, 13, v92
	v_mul_i32_i24_e32 v106, 0x6000, v106
	v_add_u32_e32 v98, v106, v64
	global_load_dwordx4 v[0:3], v94, s[48:49] nt
	global_load_dwordx4 v[4:7], v94, s[48:49] offset:1024 nt
	global_load_dwordx4 v[8:11], v94, s[48:49] offset:2048 nt
	global_load_dwordx4 v[12:15], v94, s[48:49] offset:3072 nt
	global_load_dwordx4 v[112:115], v98, s[96:97]
	global_load_dwordx4 v[120:123], v98, s[96:97] offset:1024
	global_load_dwordx4 v[128:131], v98, s[96:97] offset:2048
	global_load_dwordx4 v[136:139], v98, s[96:97] offset:3072
	global_load_dwordx4 v[116:119], v98, s[4:5]
	global_load_dwordx4 v[124:127], v98, s[4:5] offset:1024
	global_load_dwordx4 v[132:135], v98, s[4:5] offset:2048
	global_load_dwordx4 v[140:143], v98, s[4:5] offset:3072
	v_lshl_add_u32 v102, v92, 11, v70
	v_cmp_gt_i32_e32 vcc, s20, v93
	s_and_saveexec_b64 s[0:1], vcc
	v_lshl_add_u32 v95, v93, 12, v64
	v_ashrrev_i32_e32 v106, 13, v93
	v_mul_i32_i24_e32 v106, 0x6000, v106
	v_add_u32_e32 v99, v106, v64
	global_load_dwordx4 v[16:19], v95, s[48:49] nt
	global_load_dwordx4 v[20:23], v95, s[48:49] offset:1024 nt
	global_load_dwordx4 v[24:27], v95, s[48:49] offset:2048 nt
	global_load_dwordx4 v[28:31], v95, s[48:49] offset:3072 nt
	global_load_dwordx4 v[144:147], v99, s[96:97]
	global_load_dwordx4 v[152:155], v99, s[96:97] offset:1024
	global_load_dwordx4 v[160:163], v99, s[96:97] offset:2048
	global_load_dwordx4 v[168:171], v99, s[96:97] offset:3072
	global_load_dwordx4 v[148:151], v99, s[4:5]
	global_load_dwordx4 v[156:159], v99, s[4:5] offset:1024
	global_load_dwordx4 v[164:167], v99, s[4:5] offset:2048
	global_load_dwordx4 v[172:175], v99, s[4:5] offset:3072
	v_lshl_add_u32 v103, v93, 11, v70
	s_or_b64 exec, exec, s[0:1]
	v_cmp_gt_i32_e32 vcc, s20, v90
	s_and_saveexec_b64 s[0:1], vcc
	v_lshl_add_u32 v96, v90, 12, v64
	v_ashrrev_i32_e32 v106, 13, v90
	v_mul_i32_i24_e32 v106, 0x6000, v106
	v_add_u32_e32 v100, v106, v64
	global_load_dwordx4 v[32:35], v96, s[48:49] nt
	global_load_dwordx4 v[36:39], v96, s[48:49] offset:1024 nt
	global_load_dwordx4 v[40:43], v96, s[48:49] offset:2048 nt
	global_load_dwordx4 v[44:47], v96, s[48:49] offset:3072 nt
	global_load_dwordx4 v[176:179], v100, s[96:97]
	global_load_dwordx4 v[184:187], v100, s[96:97] offset:1024
	global_load_dwordx4 v[192:195], v100, s[96:97] offset:2048
	global_load_dwordx4 v[200:203], v100, s[96:97] offset:3072
	global_load_dwordx4 v[180:183], v100, s[4:5]
	global_load_dwordx4 v[188:191], v100, s[4:5] offset:1024
	global_load_dwordx4 v[196:199], v100, s[4:5] offset:2048
	global_load_dwordx4 v[204:207], v100, s[4:5] offset:3072
	v_lshl_add_u32 v104, v90, 11, v70
	s_or_b64 exec, exec, s[0:1]
	v_cmp_gt_i32_e32 vcc, s20, v88
	s_and_saveexec_b64 s[0:1], vcc
	v_lshl_add_u32 v97, v88, 12, v64
	v_ashrrev_i32_e32 v106, 13, v88
	v_mul_i32_i24_e32 v106, 0x6000, v106
	v_add_u32_e32 v101, v106, v64
	global_load_dwordx4 v[48:51], v97, s[48:49] nt
	global_load_dwordx4 v[52:55], v97, s[48:49] offset:1024 nt
	global_load_dwordx4 v[56:59], v97, s[48:49] offset:2048 nt
	global_load_dwordx4 v[60:63], v97, s[48:49] offset:3072 nt
	global_load_dwordx4 v[208:211], v101, s[96:97]
	global_load_dwordx4 v[216:219], v101, s[96:97] offset:1024
	global_load_dwordx4 v[224:227], v101, s[96:97] offset:2048
	global_load_dwordx4 v[232:235], v101, s[96:97] offset:3072
	global_load_dwordx4 v[212:215], v101, s[4:5]
	global_load_dwordx4 v[220:223], v101, s[4:5] offset:1024
	global_load_dwordx4 v[228:231], v101, s[4:5] offset:2048
	global_load_dwordx4 v[236:239], v101, s[4:5] offset:3072
	v_lshl_add_u32 v105, v88, 11, v70
	s_or_b64 exec, exec, s[0:1]
	s_waitcnt vmcnt(0)
	v_pk_add_f32 v[118:119], v[118:119], 1.0 op_sel_hi:[1,0]
	v_pk_add_f32 v[116:117], v[116:117], 1.0 op_sel_hi:[1,0]
	v_pk_add_f32 v[126:127], v[126:127], 1.0 op_sel_hi:[1,0]
	v_pk_add_f32 v[124:125], v[124:125], 1.0 op_sel_hi:[1,0]
	v_pk_add_f32 v[134:135], v[134:135], 1.0 op_sel_hi:[1,0]
	v_pk_add_f32 v[132:133], v[132:133], 1.0 op_sel_hi:[1,0]
	v_pk_add_f32 v[142:143], v[142:143], 1.0 op_sel_hi:[1,0]
	v_pk_add_f32 v[140:141], v[140:141], 1.0 op_sel_hi:[1,0]
	v_pk_fma_f32 v[2:3], v[2:3], v[118:119], v[114:115]
	v_pk_fma_f32 v[0:1], v[0:1], v[116:117], v[112:113]
	v_pk_fma_f32 v[6:7], v[6:7], v[126:127], v[122:123]
	v_pk_fma_f32 v[4:5], v[4:5], v[124:125], v[120:121]
	v_pk_fma_f32 v[10:11], v[10:11], v[134:135], v[130:131]
	v_pk_fma_f32 v[8:9], v[8:9], v[132:133], v[128:129]
	v_pk_fma_f32 v[14:15], v[14:15], v[142:143], v[138:139]
	v_pk_fma_f32 v[12:13], v[12:13], v[140:141], v[136:137]
	v_cvt_pk_bf16_f32 v0, v0, v1
	v_cvt_pk_bf16_f32 v1, v2, v3
	v_cvt_pk_bf16_f32 v4, v4, v5
	v_cvt_pk_bf16_f32 v5, v6, v7
	v_cvt_pk_bf16_f32 v8, v8, v9
	v_cvt_pk_bf16_f32 v9, v10, v11
	v_cvt_pk_bf16_f32 v12, v12, v13
	v_cvt_pk_bf16_f32 v13, v14, v15
	global_store_dwordx2 v102, v[0:1], s[18:19]
	global_store_dwordx2 v102, v[4:5], s[18:19] offset:512
	global_store_dwordx2 v102, v[8:9], s[18:19] offset:1024
	global_store_dwordx2 v102, v[12:13], s[18:19] offset:1536
	v_cmp_gt_i32_e32 vcc, s20, v93
	s_and_saveexec_b64 s[0:1], vcc
	v_pk_add_f32 v[150:151], v[150:151], 1.0 op_sel_hi:[1,0]
	v_pk_add_f32 v[148:149], v[148:149], 1.0 op_sel_hi:[1,0]
	v_pk_add_f32 v[158:159], v[158:159], 1.0 op_sel_hi:[1,0]
	v_pk_add_f32 v[156:157], v[156:157], 1.0 op_sel_hi:[1,0]
	v_pk_add_f32 v[166:167], v[166:167], 1.0 op_sel_hi:[1,0]
	v_pk_add_f32 v[164:165], v[164:165], 1.0 op_sel_hi:[1,0]
	v_pk_add_f32 v[174:175], v[174:175], 1.0 op_sel_hi:[1,0]
	v_pk_add_f32 v[172:173], v[172:173], 1.0 op_sel_hi:[1,0]
	v_pk_fma_f32 v[18:19], v[18:19], v[150:151], v[146:147]
	v_pk_fma_f32 v[16:17], v[16:17], v[148:149], v[144:145]
	v_pk_fma_f32 v[22:23], v[22:23], v[158:159], v[154:155]
	v_pk_fma_f32 v[20:21], v[20:21], v[156:157], v[152:153]
	v_pk_fma_f32 v[26:27], v[26:27], v[166:167], v[162:163]
	v_pk_fma_f32 v[24:25], v[24:25], v[164:165], v[160:161]
	v_pk_fma_f32 v[30:31], v[30:31], v[174:175], v[170:171]
	v_pk_fma_f32 v[28:29], v[28:29], v[172:173], v[168:169]
	v_cvt_pk_bf16_f32 v16, v16, v17
	v_cvt_pk_bf16_f32 v17, v18, v19
	v_cvt_pk_bf16_f32 v20, v20, v21
	v_cvt_pk_bf16_f32 v21, v22, v23
	v_cvt_pk_bf16_f32 v24, v24, v25
	v_cvt_pk_bf16_f32 v25, v26, v27
	v_cvt_pk_bf16_f32 v28, v28, v29
	v_cvt_pk_bf16_f32 v29, v30, v31
	global_store_dwordx2 v103, v[16:17], s[18:19]
	global_store_dwordx2 v103, v[20:21], s[18:19] offset:512
	global_store_dwordx2 v103, v[24:25], s[18:19] offset:1024
	global_store_dwordx2 v103, v[28:29], s[18:19] offset:1536
	s_or_b64 exec, exec, s[0:1]
	v_cmp_gt_i32_e32 vcc, s20, v90
	s_and_saveexec_b64 s[0:1], vcc
	v_pk_add_f32 v[182:183], v[182:183], 1.0 op_sel_hi:[1,0]
	v_pk_add_f32 v[180:181], v[180:181], 1.0 op_sel_hi:[1,0]
	v_pk_add_f32 v[190:191], v[190:191], 1.0 op_sel_hi:[1,0]
	v_pk_add_f32 v[188:189], v[188:189], 1.0 op_sel_hi:[1,0]
	v_pk_add_f32 v[198:199], v[198:199], 1.0 op_sel_hi:[1,0]
	v_pk_add_f32 v[196:197], v[196:197], 1.0 op_sel_hi:[1,0]
	v_pk_add_f32 v[206:207], v[206:207], 1.0 op_sel_hi:[1,0]
	v_pk_add_f32 v[204:205], v[204:205], 1.0 op_sel_hi:[1,0]
	v_pk_fma_f32 v[34:35], v[34:35], v[182:183], v[178:179]
	v_pk_fma_f32 v[32:33], v[32:33], v[180:181], v[176:177]
	v_pk_fma_f32 v[38:39], v[38:39], v[190:191], v[186:187]
	v_pk_fma_f32 v[36:37], v[36:37], v[188:189], v[184:185]
	v_pk_fma_f32 v[42:43], v[42:43], v[198:199], v[194:195]
	v_pk_fma_f32 v[40:41], v[40:41], v[196:197], v[192:193]
	v_pk_fma_f32 v[46:47], v[46:47], v[206:207], v[202:203]
	v_pk_fma_f32 v[44:45], v[44:45], v[204:205], v[200:201]
	v_cvt_pk_bf16_f32 v32, v32, v33
	v_cvt_pk_bf16_f32 v33, v34, v35
	v_cvt_pk_bf16_f32 v36, v36, v37
	v_cvt_pk_bf16_f32 v37, v38, v39
	v_cvt_pk_bf16_f32 v40, v40, v41
	v_cvt_pk_bf16_f32 v41, v42, v43
	v_cvt_pk_bf16_f32 v44, v44, v45
	v_cvt_pk_bf16_f32 v45, v46, v47
	global_store_dwordx2 v104, v[32:33], s[18:19]
	global_store_dwordx2 v104, v[36:37], s[18:19] offset:512
	global_store_dwordx2 v104, v[40:41], s[18:19] offset:1024
	global_store_dwordx2 v104, v[44:45], s[18:19] offset:1536
	s_or_b64 exec, exec, s[0:1]
	v_cmp_gt_i32_e32 vcc, s20, v88
	s_and_saveexec_b64 s[0:1], vcc
	v_pk_add_f32 v[214:215], v[214:215], 1.0 op_sel_hi:[1,0]
	v_pk_add_f32 v[212:213], v[212:213], 1.0 op_sel_hi:[1,0]
	v_pk_add_f32 v[222:223], v[222:223], 1.0 op_sel_hi:[1,0]
	v_pk_add_f32 v[220:221], v[220:221], 1.0 op_sel_hi:[1,0]
	v_pk_add_f32 v[230:231], v[230:231], 1.0 op_sel_hi:[1,0]
	v_pk_add_f32 v[228:229], v[228:229], 1.0 op_sel_hi:[1,0]
	v_pk_add_f32 v[238:239], v[238:239], 1.0 op_sel_hi:[1,0]
	v_pk_add_f32 v[236:237], v[236:237], 1.0 op_sel_hi:[1,0]
	v_pk_fma_f32 v[50:51], v[50:51], v[214:215], v[210:211]
	v_pk_fma_f32 v[48:49], v[48:49], v[212:213], v[208:209]
	v_pk_fma_f32 v[54:55], v[54:55], v[222:223], v[218:219]
	v_pk_fma_f32 v[52:53], v[52:53], v[220:221], v[216:217]
	v_pk_fma_f32 v[58:59], v[58:59], v[230:231], v[226:227]
	v_pk_fma_f32 v[56:57], v[56:57], v[228:229], v[224:225]
	v_pk_fma_f32 v[62:63], v[62:63], v[238:239], v[234:235]
	v_pk_fma_f32 v[60:61], v[60:61], v[236:237], v[232:233]
	v_cvt_pk_bf16_f32 v48, v48, v49
	v_cvt_pk_bf16_f32 v49, v50, v51
	v_cvt_pk_bf16_f32 v52, v52, v53
	v_cvt_pk_bf16_f32 v53, v54, v55
	v_cvt_pk_bf16_f32 v56, v56, v57
	v_cvt_pk_bf16_f32 v57, v58, v59
	v_cvt_pk_bf16_f32 v60, v60, v61
	v_cvt_pk_bf16_f32 v61, v62, v63
	global_store_dwordx2 v105, v[48:49], s[18:19]
	global_store_dwordx2 v105, v[52:53], s[18:19] offset:512
	global_store_dwordx2 v105, v[56:57], s[18:19] offset:1024
	global_store_dwordx2 v105, v[60:61], s[18:19] offset:1536
	s_or_b64 exec, exec, s[0:1]
	s_mov_b64 s[0:1], 0
	s_branch .LBB0_76
